# attention phase: static s_setprio 1 for waves 4-7 (reset after the phase)
# baseline (speedup 1.0000x reference)
.LBB0_1660:
	s_cmp_lt_i32 s80, 11
	s_cselect_b64 s[4:5], -1, 0
	s_and_b64 s[0:1], s[4:5], s[0:1]
	s_andn2_b64 vcc, exec, s[0:1]
	s_cbranch_vccnz .LBB0_1811
	s_cmp_lt_u32 s92, 4
	s_cbranch_scc1 .Lattn_prio_skip
	s_setprio 1
.Lattn_prio_skip:
	v_readlane_b32 s4, v253, 46
	v_mov_b32_e32 v159, 0
	v_readlane_b32 s18, v253, 60
	v_readlane_b32 s19, v253, 61
	v_or_b32_e32 v1, 1, v193
	v_mbcnt_hi_u32_b32 v7, -1, v227
	v_lshl_add_u64 v[2:3], s[18:19], 0, v[158:159]
	v_add_co_u32_e32 v2, vcc, 0x1582000, v2
	v_lshlrev_b32_e32 v6, 2, v1
	s_nop 0
	v_addc_co_u32_e32 v3, vcc, 0, v3, vcc
	global_load_dwordx2 v[2:3], v[2:3], off
	v_and_b32_e32 v4, 64, v7
	v_add_u32_e32 v9, -1, v7
	v_and_b32_e32 v8, 0x78, v158
	v_and_b32_e32 v6, 0x7c, v6
	v_cmp_lt_i32_e32 vcc, v9, v4
	v_or_b32_e32 v5, 5, v8
	s_movk_i32 s4, 0x46
	v_cndmask_b32_e32 v9, v9, v7, vcc
	v_lshlrev_b32_e32 v15, 2, v9
	v_readlane_b32 s6, v253, 48
	v_readlane_b32 s7, v253, 49
	v_readlane_b32 s5, v253, 47
	v_add_u32_e32 v10, -2, v7
	v_add_u32_e32 v11, -4, v7
	v_add_u32_e32 v12, -8, v7
	v_add_u32_e32 v13, -16, v7
	v_subrev_u32_e32 v14, 32, v7
	v_readlane_b32 s8, v253, 50
	v_readlane_b32 s9, v253, 51
	v_readlane_b32 s10, v253, 52
	v_readlane_b32 s11, v253, 53
	v_cmp_eq_u32_e64 s[8:9], 63, v82
	v_readlane_b32 s12, v253, 54
	v_readlane_b32 s13, v253, 55
	v_readlane_b32 s14, v253, 56
	v_readlane_b32 s15, v253, 57
	v_readlane_b32 s16, v253, 58
	v_readlane_b32 s17, v253, 59
	s_waitcnt vmcnt(0)
	v_sub_u32_e32 v6, v6, v3
	v_sub_u32_e32 v9, v5, v2
	v_add_u32_e32 v5, 5, v6
	v_cmp_lt_i32_e32 vcc, s4, v5
	v_cmp_lt_i32_e64 s[6:7], s4, v9
	s_nop 0
	v_cndmask_b32_e64 v16, 0, 1, vcc
	v_addc_co_u32_e64 v9, s[4:5], 0, v16, s[6:7]
	ds_bpermute_b32 v15, v15, v9
	v_cmp_lt_i32_e64 s[4:5], v10, v4
	s_nop 1
	v_cndmask_b32_e64 v10, v10, v7, s[4:5]
	v_cmp_ne_u32_e64 s[4:5], 0, v82
	v_lshlrev_b32_e32 v10, 2, v10
	s_waitcnt lgkmcnt(0)
	v_cndmask_b32_e64 v15, 0, v15, s[4:5]
	v_addc_co_u32_e64 v15, s[4:5], v15, v16, s[6:7]
	ds_bpermute_b32 v10, v10, v15
	v_cmp_lt_i32_e64 s[4:5], v11, v4
	s_nop 1
	v_cndmask_b32_e64 v11, v11, v7, s[4:5]
	v_cmp_lt_u32_e64 s[4:5], 1, v82
	v_lshlrev_b32_e32 v11, 2, v11
	s_waitcnt lgkmcnt(0)
	v_cndmask_b32_e64 v10, 0, v10, s[4:5]
	v_add_u32_e32 v10, v10, v15
	ds_bpermute_b32 v11, v11, v10
	v_cmp_lt_i32_e64 s[4:5], v12, v4
	s_nop 1
	v_cndmask_b32_e64 v12, v12, v7, s[4:5]
	v_cmp_lt_u32_e64 s[4:5], 3, v82
	v_lshlrev_b32_e32 v12, 2, v12
	s_waitcnt lgkmcnt(0)
	v_cndmask_b32_e64 v11, 0, v11, s[4:5]
	v_add_u32_e32 v10, v11, v10
	ds_bpermute_b32 v11, v12, v10
	v_cmp_lt_i32_e64 s[4:5], v13, v4
	s_nop 1
	v_cndmask_b32_e64 v12, v13, v7, s[4:5]
	v_cmp_lt_u32_e64 s[4:5], 7, v82
	v_lshlrev_b32_e32 v12, 2, v12
	s_waitcnt lgkmcnt(0)
	v_cndmask_b32_e64 v11, 0, v11, s[4:5]
	v_add_u32_e32 v10, v11, v10
	ds_bpermute_b32 v11, v12, v10
	v_cmp_lt_i32_e64 s[4:5], v14, v4
	s_nop 1
	v_cndmask_b32_e64 v12, v14, v7, s[4:5]
	v_cmp_lt_u32_e64 s[4:5], 15, v82
	v_lshlrev_b32_e32 v12, 2, v12
	s_waitcnt lgkmcnt(0)
	v_cndmask_b32_e64 v11, 0, v11, s[4:5]
	v_add_u32_e32 v10, v11, v10
	ds_bpermute_b32 v11, v12, v10
	v_cmp_gt_u32_e64 s[4:5], 32, v82
	s_waitcnt lgkmcnt(0)
	s_nop 0
	v_cndmask_b32_e64 v11, v11, 0, s[4:5]
	v_add_u32_e32 v10, v11, v10
	s_and_saveexec_b64 s[10:11], s[8:9]
	s_lshl_b32 s8, s92, 2
	s_add_i32 s8, s8, 0
	s_add_i32 s8, s8, 0x20500
	v_mov_b32_e32 v11, s8
	ds_write_b32 v11, v10
	s_or_b64 exec, exec, s[10:11]
	s_cmp_lt_u32 s77, 64
	s_waitcnt lgkmcnt(0)
	s_barrier
	s_cbranch_scc1 .LBB0_1671
	s_add_i32 s8, 0, 0x20500
	v_mov_b32_e32 v11, s8
	ds_read_b32 v159, v11
	s_cmpk_lt_u32 s77, 0x80
	v_mov_b32_e32 v11, 0
	v_mov_b32_e32 v12, 0
	s_cbranch_scc0 .LBB0_1672

.LBB0_1811:
	s_setprio 0
	s_cmp_gt_i32 s81, 11
	s_cselect_b64 s[4:5], -1, 0
	s_and_b64 s[0:1], s[0:1], s[4:5]
	v_readlane_b32 s36, v253, 46
	s_andn2_b64 vcc, exec, s[0:1]
	v_readlane_b32 s37, v253, 47
	v_readlane_b32 s38, v253, 48
	v_readlane_b32 s39, v253, 49
	v_readlane_b32 s40, v253, 50
	v_readlane_b32 s41, v253, 51
	v_readlane_b32 s48, v253, 58
	v_readlane_b32 s49, v253, 59
	v_readlane_b32 s50, v253, 60
	v_readlane_b32 s51, v253, 61
	v_readlane_b32 s42, v253, 52
	v_readlane_b32 s43, v253, 53
	v_readlane_b32 s44, v253, 54
	v_readlane_b32 s45, v253, 55
	v_readlane_b32 s46, v253, 56
	v_readlane_b32 s47, v253, 57
	s_cbranch_vccnz .LBB0_1865
	s_waitcnt vmcnt(0)
	s_waitcnt lgkmcnt(0)
	s_barrier
	s_and_saveexec_b64 s[0:1], s[78:79]
	s_cbranch_execz .LBB0_1864
	v_mov_b32_e32 v1, 0x22160
	s_waitcnt vmcnt(0) lgkmcnt(0)
	ds_read_b32 v2, v1
	v_mov_b32_e32 v3, 1
	v_mov_b32_e32 v4, s99
	v_and_b32_e32 v5, 0xffff, v4
	v_lshrrev_b32_e32 v6, 16, v4
	global_atomic_add v7, v5, v3, s[100:101] sc0
	buffer_inv sc1
	v_lshrrev_b32_e32 v8, 8, v5
	v_sub_u32_e32 v8, s98, v8
	v_add_u32_e32 v8, 7, v8
	v_lshrrev_b32_e32 v8, 3, v8
	v_mov_b32_e32 v9, s98
	v_min_u32_e32 v9, 8, v9
	v_mov_b32_e32 v10, 0
	s_waitcnt lgkmcnt(0)
	v_add_u32_e32 v2, 1, v2
	ds_write_b32 v1, v2
	v_mul_lo_u32 v8, v8, v2
	v_mul_lo_u32 v9, v9, v2
	s_waitcnt vmcnt(0)
	v_add_u32_e32 v7, 1, v7
	v_cmp_eq_u32_e32 vcc, v7, v8
	s_cbranch_vccz .Lgb_poll_11
	v_mov_b32_e32 v4, 0
	global_atomic_add v4, v3, s[100:101] offset:2048
	global_atomic_add v4, v3, s[100:101] offset:2304
	global_atomic_add v4, v3, s[100:101] offset:2560
	global_atomic_add v4, v3, s[100:101] offset:2816
	global_atomic_add v4, v3, s[100:101] offset:3072
	global_atomic_add v4, v3, s[100:101] offset:3328
	global_atomic_add v4, v3, s[100:101] offset:3584
	global_atomic_add v4, v3, s[100:101] offset:3840
